# v21
# speedup vs baseline: 1.0899x; 1.0899x over previous
_Z8k_layer1PKiS0_PKfS2_PK15HIP_vector_typeIjLj4EEPKDv8_DF16_S9_S2_S2_S2_PDF16_PfSB_:
	s_load_dwordx2 s[14:15], s[0:1], 0x48
	s_load_dwordx8 s[4:11], s[0:1], 0x28
	v_readfirstlane_b32 s13, v0
	s_lshr_b32 s12, s13, 6
	v_and_b32_e32 v178, 63, v0
	v_lshl_or_b32 v2, s12, 10, v178
	v_ashrrev_i32_e32 v3, 31, v2
	v_lshlrev_b64 v[4:5], 4, v[2:3]
	s_waitcnt lgkmcnt(0)
	v_lshl_add_u64 v[6:7], s[6:7], 0, v[4:5]
	s_movk_i32 s3, 0x1000
	v_add_co_u32_e32 v8, vcc, s3, v6
	s_movk_i32 s6, 0x2000
	s_nop 0
	v_addc_co_u32_e32 v9, vcc, 0, v7, vcc
	v_add_co_u32_e32 v10, vcc, s6, v6
	s_movk_i32 s6, 0x3000
	s_nop 0
	v_addc_co_u32_e32 v11, vcc, 0, v7, vcc
	global_load_dwordx4 v[32:35], v[6:7], off
	global_load_dwordx4 v[36:39], v[6:7], off offset:1024
	global_load_dwordx4 v[40:43], v[6:7], off offset:2048
	global_load_dwordx4 v[44:47], v[6:7], off offset:3072
	v_add_co_u32_e32 v6, vcc, s6, v6
	v_lshl_add_u64 v[4:5], s[4:5], 0, v[4:5]
	s_nop 0
	v_addc_co_u32_e32 v7, vcc, 0, v7, vcc
	v_or_b32_e32 v2, 0x200, v2
	global_load_dwordx4 v[48:51], v[8:9], off offset:1024
	global_load_dwordx4 v[52:55], v[8:9], off offset:2048
	global_load_dwordx4 v[56:59], v[10:11], off offset:-4096
	global_load_dwordx4 v[60:63], v[10:11], off
	global_load_dwordx4 v[64:67], v[10:11], off offset:1024
	global_load_dwordx4 v[68:71], v[10:11], off offset:2048
	global_load_dwordx4 v[72:75], v[10:11], off offset:3072
	global_load_dwordx4 v[76:79], v[8:9], off offset:3072
	global_load_dwordx4 v[80:83], v[6:7], off
	global_load_dwordx4 v[84:87], v[6:7], off offset:1024
	global_load_dwordx4 v[88:91], v[6:7], off offset:2048
	global_load_dwordx4 v[92:95], v[6:7], off offset:3072
	v_add_co_u32_e32 v6, vcc, s3, v4
	v_ashrrev_i32_e32 v3, 31, v2
	s_nop 0
	v_addc_co_u32_e32 v7, vcc, 0, v5, vcc
	v_lshl_add_u64 v[2:3], v[2:3], 4, s[4:5]
	global_load_dwordx4 v[96:99], v[4:5], off
	global_load_dwordx4 v[100:103], v[4:5], off offset:1024
	global_load_dwordx4 v[104:107], v[4:5], off offset:2048
	global_load_dwordx4 v[108:111], v[4:5], off offset:3072
	global_load_dwordx4 v[112:115], v[6:7], off
	global_load_dwordx4 v[116:119], v[6:7], off offset:1024
	global_load_dwordx4 v[120:123], v[6:7], off offset:2048
	global_load_dwordx4 v[124:127], v[6:7], off offset:3072
	global_load_dwordx4 v[128:131], v[2:3], off
	global_load_dwordx4 v[132:135], v[2:3], off offset:1024
	global_load_dwordx4 v[136:139], v[2:3], off offset:2048
	global_load_dwordx4 v[140:143], v[2:3], off offset:3072
	v_add_co_u32_e32 v2, vcc, s6, v4
	s_lshl_b32 s3, s12, 4
	s_nop 0
	v_addc_co_u32_e32 v3, vcc, 0, v5, vcc
	global_load_dwordx4 v[144:147], v[2:3], off
	global_load_dwordx4 v[148:151], v[2:3], off offset:1024
	global_load_dwordx4 v[152:155], v[2:3], off offset:2048
	global_load_dwordx4 v[156:159], v[2:3], off offset:3072
	v_and_or_b32 v1, v0, 15, s3
	v_lshlrev_b32_e32 v1, 2, v1
	global_load_dword v179, v1, s[10:11]
	global_load_dword v180, v1, s[14:15]
	v_bfe_u32 v2, v0, 4, 2
	s_lshl_b32 s16, s3, 2
	v_lshl_add_u32 v2, v2, 4, s16
	global_load_dwordx4 v[228:231], v2, s[10:11]
	global_load_dwordx4 v[232:235], v2, s[14:15]
	v_cmp_gt_u32_e32 vcc, 32, v0
	v_lshlrev_b32_e32 v0, 2, v0
	s_and_saveexec_b64 s[4:5], vcc
	v_mov_b32_e32 v1, 0
	v_add_u32_e32 v2, 0xd000, v0
	ds_write2_b32 v2, v1, v1 offset0:176 offset1:208
	s_or_b64 exec, exec, s[4:5]
	global_load_dword v1, v0, s[8:9]
	global_load_dword v2, v0, s[8:9] offset:1024
	s_cmpk_gt_i32 s2, 0x61a
	s_waitcnt vmcnt(0)
	ds_write2st64_b32 v0, v1, v2 offset0:202 offset1:206
	s_waitcnt lgkmcnt(0)
	s_barrier
	s_cbranch_scc1 .LBB3_271
	s_load_dwordx8 s[56:63], s[0:1], 0x0
	s_load_dwordx4 s[4:7], s[0:1], 0x50
	s_mul_i32 s87, s12, 48
	s_lshl_b32 s66, s12, 9
	s_and_b32 s65, s13, 0xffffffc0
	s_lshl_b32 s86, s12, 3
	s_waitcnt lgkmcnt(0)
	v_writelane_b32 v226, s4, 0
	s_add_i32 s87, s87, 0xd200
	s_add_i32 s90, s66, 0xc200
	v_writelane_b32 v226, s5, 1
	v_writelane_b32 v226, s6, 2
	v_writelane_b32 v226, s7, 3
	s_lshl_b32 s4, s12, 12
	s_add_i32 s88, s4, 0x8200
	s_lshl_b32 s5, s12, 1
	s_load_dwordx2 s[72:73], s[0:1], 0x20
	s_load_dwordx2 s[76:77], s[0:1], 0x60
	s_add_u32 s0, s0, 0x68
	s_addc_u32 s1, s1, 0
	v_mbcnt_lo_u32_b32 v0, -1, 0
	v_writelane_b32 v226, s0, 4
	v_mbcnt_hi_u32_b32 v182, -1, v0
	s_mul_i32 s99, s12, 0x2080
	v_writelane_b32 v226, s1, 5
	s_or_b32 s0, s5, 1
	v_and_b32_e32 v0, 64, v182
	s_mov_b32 s91, 0xff800000
	s_lshl_b32 s95, s12, 8
	s_lshl_b32 s64, s0, 8
	s_lshl_b32 s98, s0, 7
	s_add_i32 s93, s4, 0x8500
	s_or_b32 s92, s99, 48
	s_mov_b32 s68, 0
	v_mov_b32_e32 v177, 0
	v_mov_b32_e32 v181, 0xff800000
	s_movk_i32 s69, 0x410
	v_xor_b32_e32 v183, 32, v182
	v_add_u32_e32 v184, 64, v0
	v_xor_b32_e32 v185, 4, v182
	v_xor_b32_e32 v186, 8, v182
	v_xor_b32_e32 v187, 16, v182
	v_mov_b32_e32 v188, 0x3c0
	v_writelane_b32 v226, s92, 6
	s_lshl_b32 s0, s2, 5
	s_add_i32 s0, s0, s86
	v_min_i32_e32 v1, 8, v178
	v_add_u32_e32 v1, s0, v1
	v_min_i32_e32 v1, 0xc350, v1
	v_lshlrev_b32_e32 v1, 2, v1
	global_load_dword v236, v1, s[56:57]
	s_waitcnt vmcnt(0)
	s_branch .LBB3_6

.LBB3_5:
	s_or_b64 exec, exec, s[0:1]
	s_addk_i32 s2, 0x200
	s_cmpk_gt_i32 s2, 0x61a
	s_cbranch_scc1 .LBB3_271
.LBB3_6:
	v_mov_b32_e32 v189, v178
	s_lshl_b32 s74, s2, 5
	s_add_i32 s22, s74, s86
	s_waitcnt vmcnt(2)
	v_mov_b32_e32 v0, v236
	s_add_i32 s0, s2, 0x200
	s_cmpk_gt_i32 s0, 0x61a
	s_cbranch_scc1 .Lk4_nopf
	s_lshl_b32 s0, s0, 5
	s_add_i32 s0, s0, s86
	v_min_i32_e32 v1, 8, v189
	v_add_u32_e32 v1, s0, v1
	v_min_i32_e32 v1, 0xc350, v1
	v_lshlrev_b32_e32 v1, 2, v1
	global_load_dword v236, v1, s[56:57]
.Lk4_nopf:
	v_cmp_gt_i32_e32 vcc, 9, v189
	s_and_saveexec_b64 s[0:1], vcc
	s_cbranch_execz .LBB3_8
	v_lshl_add_u32 v1, v189, 2, s87
	ds_write_b32 v1, v0
.LBB3_8:
	s_or_b64 exec, exec, s[0:1]
	v_readlane_b32 s0, v0, 8
	v_readlane_b32 s1, v0, 2
	v_readlane_b32 s78, v0, 0
	v_readlane_b32 s4, v0, 4
	v_readlane_b32 s5, v0, 6
	s_sub_i32 s33, s1, s78
	s_sub_i32 s96, s4, s1
	s_sub_i32 s97, s5, s4
	s_sub_i32 s75, s0, s5
	s_max_i32 s1, s33, s96
	v_mov_b32_e32 v0, s97
	v_mov_b32_e32 v1, s75
	s_sub_i32 s23, s0, s78
	v_max3_i32 v166, s1, v0, v1
	s_cmpk_gt_i32 s23, 0x80
	s_cselect_b64 s[0:1], -1, 0
	v_cmp_lt_i32_e32 vcc, 64, v166
	s_or_b64 s[4:5], s[0:1], vcc
	s_mov_b64 s[0:1], -1
	s_and_b64 vcc, exec, s[4:5]
	v_lshlrev_b32_e32 v165, 3, v189
	v_ashrrev_i32_e32 v190, 2, v189
	v_ashrrev_i32_e32 v191, 5, v189
	v_and_b32_e32 v192, 31, v189
	s_cbranch_vccz .LBB3_86
	v_cmp_lt_i32_e32 vcc, v183, v184
	v_and_b32_e32 v169, 3, v189
	v_ashrrev_i32_e32 v168, 5, v189
	v_cndmask_b32_e32 v0, v182, v183, vcc
	v_lshlrev_b32_e32 v170, 2, v0
	v_and_b32_e32 v0, 0xffffffe0, v189
	v_cmp_lt_i32_e32 vcc, v185, v184
	v_add_u32_e32 v174, s88, v0
	v_ashrrev_i32_e32 v164, 2, v189
	v_cndmask_b32_e32 v0, v182, v185, vcc
	v_cmp_lt_i32_e32 vcc, v186, v184
	v_lshlrev_b32_e32 v175, 2, v0
	v_and_b32_e32 v167, 31, v189
	v_cndmask_b32_e32 v0, v182, v186, vcc
	v_cmp_lt_i32_e32 vcc, v187, v184
	v_lshl_add_u32 v172, v169, 3, s88
	v_lshlrev_b32_e32 v193, 2, v0
	v_cndmask_b32_e32 v0, v182, v187, vcc
	v_lshlrev_b32_e32 v196, 7, v168
	v_cmp_gt_u32_e64 s[0:1], 4, v189
	v_cmp_gt_u32_e64 s[4:5], 32, v189
	s_mov_b32 s24, 0
	v_lshlrev_b32_e32 v171, 2, v167
	v_lshl_add_u32 v173, v164, 5, v172
	v_lshlrev_b32_e32 v194, 2, v0
	v_lshl_add_u32 v195, v168, 2, s88
	v_add_u32_e32 v197, 0x100, v196
	v_add_u32_e32 v198, 0x200, v196
	v_add_u32_e32 v199, 0x300, v196
	v_add_u32_e32 v200, s88, v165
	s_branch .LBB3_11

.LBB3_222:
	v_lshlrev_b32_e32 v0, 4, v168
	v_add_u32_e32 v165, 0xca00, v0
	v_mad_u32_u24 v166, v167, s69, v0
	v_add_u32_e32 v12, s66, v165
	s_waitcnt lgkmcnt(0)
	s_barrier
	ds_read_b128 v[16:19], v12
	ds_read_b128 v[20:23], v12 offset:32
	ds_read_b128 v[24:27], v12 offset:64
	ds_read_b128 v[28:31], v12 offset:96
	v_add_u32_e32 v169, s95, v166
	ds_read_b128 v[160:163], v169
	ds_read_b128 v[170:173], v169 offset:32
	s_waitcnt lgkmcnt(1)
	v_mfma_f32_32x32x16_f16 v[16:31], v[96:99], v[160:163], v[16:31]
	ds_read_b128 v[0:3], v12 offset:128
	ds_read_b128 v[4:7], v12 offset:160
	ds_read_b128 v[8:11], v12 offset:192
	ds_read_b128 v[12:15], v12 offset:224
	v_lshlrev_b32_e32 v168, 3, v168
	v_mad_u32_u24 v174, v167, s69, v168
	v_add_u32_e32 v167, s95, v174
	s_mov_b32 s8, 0xc34f
	s_waitcnt lgkmcnt(4)
	v_mfma_f32_32x32x16_f16 v[16:31], v[100:103], v[170:173], v[16:31]
	s_waitcnt lgkmcnt(0)
	v_mfma_f32_32x32x16_f16 v[0:15], v[112:115], v[160:163], v[0:15]
	ds_read_b128 v[160:163], v169 offset:64
	ds_read_b128 v[190:193], v169 offset:96
	s_waitcnt lgkmcnt(1)
	v_mfma_f32_32x32x16_f16 v[16:31], v[104:107], v[160:163], v[16:31]
	v_mfma_f32_32x32x16_f16 v[0:15], v[116:119], v[170:173], v[0:15]
	s_waitcnt lgkmcnt(0)
	v_mfma_f32_32x32x16_f16 v[16:31], v[108:111], v[190:193], v[16:31]
	v_mfma_f32_32x32x16_f16 v[0:15], v[120:123], v[160:163], v[0:15]
	s_nop 10
	v_max_f32_e32 v17, v17, v17
	v_max_f32_e32 v18, v18, v18
	v_max_f32_e32 v19, v19, v19
	v_max_f32_e32 v16, v16, v16
	v_max_f32_e32 v20, v20, v20
	v_max_f32_e32 v21, v21, v21
	v_max_f32_e32 v22, v22, v22
	v_max_f32_e32 v168, 0, v17
	v_max_f32_e32 v17, 0, v18
	v_max_f32_e32 v18, 0, v19
	v_max_f32_e32 v19, v23, v23
	v_max_f32_e32 v16, 0, v16
	v_max_f32_e32 v20, 0, v20
	v_max_f32_e32 v21, 0, v21
	v_cvt_pk_f16_f32 v17, v17, v18
	v_max_f32_e32 v18, 0, v22
	v_max_f32_e32 v19, 0, v19
	v_mfma_f32_32x32x16_f16 v[0:15], v[124:127], v[190:193], v[0:15]
	v_cvt_pk_f16_f32 v16, v16, v168
	v_cvt_pk_f16_f32 v19, v18, v19
	v_cvt_pk_f16_f32 v18, v20, v21
	ds_write2_b64 v167, v[16:17], v[18:19] offset1:2
	v_max_f32_e32 v17, v25, v25
	v_max_f32_e32 v18, 0, v17
	v_max_f32_e32 v17, v26, v26
	v_max_f32_e32 v19, v27, v27
	v_max_f32_e32 v16, v24, v24
	v_max_f32_e32 v17, 0, v17
	v_max_f32_e32 v19, 0, v19
	v_max_f32_e32 v16, 0, v16
	v_cvt_pk_f16_f32 v17, v17, v19
	v_max_f32_e32 v19, v29, v29
	v_cvt_pk_f16_f32 v16, v16, v18
	v_max_f32_e32 v18, v28, v28
	v_max_f32_e32 v20, 0, v19
	v_max_f32_e32 v19, v30, v30
	v_max_f32_e32 v21, v31, v31
	v_max_f32_e32 v18, 0, v18
	v_max_f32_e32 v19, 0, v19
	v_max_f32_e32 v21, 0, v21
	v_cvt_pk_f16_f32 v19, v19, v21
	v_cvt_pk_f16_f32 v18, v18, v20
	v_max_f32_e32 v1, v1, v1
	ds_write2_b64 v167, v[16:17], v[18:19] offset0:4 offset1:6
	v_max_f32_e32 v16, 0, v1
	v_max_f32_e32 v1, v2, v2
	v_max_f32_e32 v2, v3, v3
	v_max_f32_e32 v1, 0, v1
	v_max_f32_e32 v2, 0, v2
	v_max_f32_e32 v3, v5, v5
	v_max_f32_e32 v0, v0, v0
	v_cvt_pk_f16_f32 v1, v1, v2
	v_max_f32_e32 v2, v4, v4
	v_max_f32_e32 v4, 0, v3
	v_max_f32_e32 v3, v6, v6
	v_max_f32_e32 v5, v7, v7
	v_max_f32_e32 v0, 0, v0
	v_max_f32_e32 v2, 0, v2
	v_max_f32_e32 v3, 0, v3
	v_max_f32_e32 v5, 0, v5
	v_cvt_pk_f16_f32 v0, v0, v16
	v_cvt_pk_f16_f32 v3, v3, v5
	v_cvt_pk_f16_f32 v2, v2, v4
	ds_write2_b64 v167, v[0:1], v[2:3] offset0:8 offset1:10
	v_max_f32_e32 v1, v9, v9
	v_max_f32_e32 v2, 0, v1
	v_max_f32_e32 v1, v10, v10
	v_max_f32_e32 v3, v11, v11
	v_max_f32_e32 v0, v8, v8
	v_max_f32_e32 v1, 0, v1
	v_max_f32_e32 v3, 0, v3
	v_max_f32_e32 v0, 0, v0
	v_cvt_pk_f16_f32 v1, v1, v3
	v_max_f32_e32 v3, v13, v13
	v_cvt_pk_f16_f32 v0, v0, v2
	v_max_f32_e32 v2, v12, v12
	v_max_f32_e32 v4, 0, v3
	v_max_f32_e32 v3, v14, v14
	v_max_f32_e32 v5, v15, v15
	v_max_f32_e32 v2, 0, v2
	v_max_f32_e32 v3, 0, v3
	v_max_f32_e32 v5, 0, v5
	v_cvt_pk_f16_f32 v3, v3, v5
	v_cvt_pk_f16_f32 v2, v2, v4
	ds_write2_b64 v167, v[0:1], v[2:3] offset0:12 offset1:14
	v_add_u32_e32 v12, s64, v165
	ds_read_b128 v[16:19], v12
	ds_read_b128 v[20:23], v12 offset:32
	ds_read_b128 v[24:27], v12 offset:64
	ds_read_b128 v[28:31], v12 offset:96
	v_add_u32_e32 v165, s98, v166
	ds_read_b128 v[160:163], v165
	ds_read_b128 v[166:169], v165 offset:32
	ds_read_b128 v[0:3], v12 offset:128
	ds_read_b128 v[4:7], v12 offset:160
	ds_read_b128 v[8:11], v12 offset:192
	ds_read_b128 v[12:15], v12 offset:224
	s_waitcnt lgkmcnt(5)
	v_mfma_f32_32x32x16_f16 v[16:31], v[128:131], v[160:163], v[16:31]
	s_waitcnt lgkmcnt(0)
	v_mfma_f32_32x32x16_f16 v[0:15], v[144:147], v[160:163], v[0:15]
	v_mfma_f32_32x32x16_f16 v[16:31], v[132:135], v[166:169], v[16:31]
	v_mfma_f32_32x32x16_f16 v[0:15], v[148:151], v[166:169], v[0:15]
	ds_read_b128 v[160:163], v165 offset:64
	ds_read_b128 v[166:169], v165 offset:96
	s_waitcnt lgkmcnt(1)
	v_mfma_f32_32x32x16_f16 v[16:31], v[136:139], v[160:163], v[16:31]
	s_waitcnt lgkmcnt(0)
	v_mfma_f32_32x32x16_f16 v[16:31], v[140:143], v[166:169], v[16:31]
	v_mfma_f32_32x32x16_f16 v[0:15], v[152:155], v[160:163], v[0:15]
	s_nop 10
	v_max_f32_e32 v17, v17, v17
	v_max_f32_e32 v161, 0, v17
	v_max_f32_e32 v17, v18, v18
	v_max_f32_e32 v18, v19, v19
	v_max_f32_e32 v17, 0, v17
	v_max_f32_e32 v18, 0, v18
	v_max_f32_e32 v19, v21, v21
	v_max_f32_e32 v16, v16, v16
	v_cvt_pk_f16_f32 v17, v17, v18
	v_max_f32_e32 v18, v20, v20
	v_max_f32_e32 v20, 0, v19
	v_max_f32_e32 v19, v22, v22
	v_max_f32_e32 v21, v23, v23
	v_mfma_f32_32x32x16_f16 v[0:15], v[156:159], v[166:169], v[0:15]
	v_max_f32_e32 v16, 0, v16
	v_max_f32_e32 v18, 0, v18
	v_max_f32_e32 v19, 0, v19
	v_max_f32_e32 v21, 0, v21
	v_add_u32_e32 v160, s98, v174
	v_cvt_pk_f16_f32 v16, v16, v161
	v_cvt_pk_f16_f32 v19, v19, v21
	v_cvt_pk_f16_f32 v18, v18, v20
	ds_write2_b64 v160, v[16:17], v[18:19] offset1:2
	v_max_f32_e32 v17, v25, v25
	v_max_f32_e32 v18, 0, v17
	v_max_f32_e32 v17, v26, v26
	v_max_f32_e32 v19, v27, v27
	v_max_f32_e32 v16, v24, v24
	v_max_f32_e32 v17, 0, v17
	v_max_f32_e32 v19, 0, v19
	v_max_f32_e32 v16, 0, v16
	v_cvt_pk_f16_f32 v17, v17, v19
	v_max_f32_e32 v19, v29, v29
	v_cvt_pk_f16_f32 v16, v16, v18
	v_max_f32_e32 v18, v28, v28
	v_max_f32_e32 v20, 0, v19
	v_max_f32_e32 v19, v30, v30
	v_max_f32_e32 v21, v31, v31
	v_max_f32_e32 v18, 0, v18
	v_max_f32_e32 v19, 0, v19
	v_max_f32_e32 v21, 0, v21
	v_cvt_pk_f16_f32 v19, v19, v21
	v_cvt_pk_f16_f32 v18, v18, v20
	v_max_f32_e32 v1, v1, v1
	ds_write2_b64 v160, v[16:17], v[18:19] offset0:4 offset1:6
	v_max_f32_e32 v16, 0, v1
	v_max_f32_e32 v1, v2, v2
	v_max_f32_e32 v2, v3, v3
	v_max_f32_e32 v1, 0, v1
	v_max_f32_e32 v2, 0, v2
	v_max_f32_e32 v3, v5, v5
	v_max_f32_e32 v0, v0, v0
	v_cvt_pk_f16_f32 v1, v1, v2
	v_max_f32_e32 v2, v4, v4
	v_max_f32_e32 v4, 0, v3
	v_max_f32_e32 v3, v6, v6
	v_max_f32_e32 v5, v7, v7
	v_max_f32_e32 v0, 0, v0
	v_max_f32_e32 v2, 0, v2
	v_max_f32_e32 v3, 0, v3
	v_max_f32_e32 v5, 0, v5
	v_cvt_pk_f16_f32 v0, v0, v16
	v_cvt_pk_f16_f32 v3, v3, v5
	v_cvt_pk_f16_f32 v2, v2, v4
	ds_write2_b64 v160, v[0:1], v[2:3] offset0:8 offset1:10
	v_max_f32_e32 v1, v9, v9
	v_max_f32_e32 v2, 0, v1
	v_max_f32_e32 v1, v10, v10
	v_max_f32_e32 v3, v11, v11
	v_max_f32_e32 v0, v8, v8
	v_max_f32_e32 v1, 0, v1
	v_max_f32_e32 v3, 0, v3
	v_max_f32_e32 v0, 0, v0
	v_cvt_pk_f16_f32 v1, v1, v3
	v_max_f32_e32 v3, v13, v13
	v_cvt_pk_f16_f32 v0, v0, v2
	v_max_f32_e32 v2, v12, v12
	v_max_f32_e32 v4, 0, v3
	v_max_f32_e32 v3, v14, v14
	v_max_f32_e32 v5, v15, v15
	v_max_f32_e32 v2, 0, v2
	v_max_f32_e32 v3, 0, v3
	v_max_f32_e32 v5, 0, v5
	v_cvt_pk_f16_f32 v3, v3, v5
	v_cvt_pk_f16_f32 v2, v2, v4
	v_mad_u32_u24 v12, v195, s69, v196
	ds_write2_b64 v160, v[0:1], v[2:3] offset0:12 offset1:14
	s_waitcnt lgkmcnt(0)
	s_barrier
	v_mul_u32_u24_e32 v16, 0x410, v195
	v_add_u32_e32 v16, v196, v16
	ds_read_b128 v[8:11], v16
	ds_read_b128 v[12:15], v16 offset:16640
	ds_read_b128 v[20:23], v16 offset:64
	ds_read_b128 v[24:27], v16 offset:16704
	ds_read_b128 v[28:31], v16 offset:128
	ds_read_b128 v[160:163], v16 offset:16768
	ds_read_b128 v[164:167], v16 offset:192
	ds_read_b128 v[168:171], v16 offset:16832
	s_waitcnt lgkmcnt(7)
	v_mfma_f32_16x16x32_f16 v[0:3], v[32:35], v[8:11], 0
	ds_read_b128 v[8:11], v16 offset:256
	s_waitcnt lgkmcnt(7)
	v_mfma_f32_16x16x32_f16 v[4:7], v[32:35], v[12:15], 0
	ds_read_b128 v[12:15], v16 offset:16896
	s_waitcnt lgkmcnt(7)
	v_mfma_f32_16x16x32_f16 v[0:3], v[36:39], v[20:23], v[0:3]
	ds_read_b128 v[20:23], v16 offset:320
	s_waitcnt lgkmcnt(7)
	v_mfma_f32_16x16x32_f16 v[4:7], v[36:39], v[24:27], v[4:7]
	ds_read_b128 v[24:27], v16 offset:16960
	s_waitcnt lgkmcnt(7)
	v_mfma_f32_16x16x32_f16 v[0:3], v[40:43], v[28:31], v[0:3]
	ds_read_b128 v[28:31], v16 offset:384
	s_waitcnt lgkmcnt(7)
	v_mfma_f32_16x16x32_f16 v[4:7], v[40:43], v[160:163], v[4:7]
	ds_read_b128 v[160:163], v16 offset:17024
	s_waitcnt lgkmcnt(7)
	v_mfma_f32_16x16x32_f16 v[0:3], v[44:47], v[164:167], v[0:3]
	ds_read_b128 v[164:167], v16 offset:448
	s_waitcnt lgkmcnt(7)
	v_mfma_f32_16x16x32_f16 v[4:7], v[44:47], v[168:171], v[4:7]
	ds_read_b128 v[168:171], v16 offset:17088
	s_waitcnt lgkmcnt(7)
	v_mfma_f32_16x16x32_f16 v[0:3], v[56:59], v[8:11], v[0:3]
	ds_read_b128 v[8:11], v16 offset:512
	s_waitcnt lgkmcnt(7)
	v_mfma_f32_16x16x32_f16 v[4:7], v[56:59], v[12:15], v[4:7]
	ds_read_b128 v[12:15], v16 offset:17152
	s_waitcnt lgkmcnt(7)
	v_mfma_f32_16x16x32_f16 v[0:3], v[48:51], v[20:23], v[0:3]
	ds_read_b128 v[20:23], v16 offset:576
	s_waitcnt lgkmcnt(7)
	v_mfma_f32_16x16x32_f16 v[4:7], v[48:51], v[24:27], v[4:7]
	ds_read_b128 v[24:27], v16 offset:17216
	s_waitcnt lgkmcnt(7)
	v_mfma_f32_16x16x32_f16 v[0:3], v[52:55], v[28:31], v[0:3]
	ds_read_b128 v[28:31], v16 offset:640
	s_waitcnt lgkmcnt(7)
	v_mfma_f32_16x16x32_f16 v[4:7], v[52:55], v[160:163], v[4:7]
	ds_read_b128 v[160:163], v16 offset:17280
	s_waitcnt lgkmcnt(7)
	v_mfma_f32_16x16x32_f16 v[0:3], v[76:79], v[164:167], v[0:3]
	ds_read_b128 v[164:167], v16 offset:704
	s_waitcnt lgkmcnt(7)
	v_mfma_f32_16x16x32_f16 v[4:7], v[76:79], v[168:171], v[4:7]
	ds_read_b128 v[168:171], v16 offset:17344
	s_waitcnt lgkmcnt(7)
	v_mfma_f32_16x16x32_f16 v[0:3], v[60:63], v[8:11], v[0:3]
	ds_read_b128 v[8:11], v16 offset:768
	s_waitcnt lgkmcnt(7)
	v_mfma_f32_16x16x32_f16 v[4:7], v[60:63], v[12:15], v[4:7]
	ds_read_b128 v[12:15], v16 offset:17408
	s_waitcnt lgkmcnt(7)
	v_mfma_f32_16x16x32_f16 v[0:3], v[64:67], v[20:23], v[0:3]
	ds_read_b128 v[20:23], v16 offset:832
	s_waitcnt lgkmcnt(7)
	v_mfma_f32_16x16x32_f16 v[4:7], v[64:67], v[24:27], v[4:7]
	ds_read_b128 v[24:27], v16 offset:17472
	s_waitcnt lgkmcnt(7)
	v_mfma_f32_16x16x32_f16 v[0:3], v[68:71], v[28:31], v[0:3]
	ds_read_b128 v[28:31], v16 offset:896
	s_waitcnt lgkmcnt(7)
	v_mfma_f32_16x16x32_f16 v[4:7], v[68:71], v[160:163], v[4:7]
	ds_read_b128 v[160:163], v16 offset:17536
	s_waitcnt lgkmcnt(7)
	v_mfma_f32_16x16x32_f16 v[0:3], v[72:75], v[164:167], v[0:3]
	ds_read_b128 v[164:167], v16 offset:960
	s_waitcnt lgkmcnt(7)
	v_mfma_f32_16x16x32_f16 v[4:7], v[72:75], v[168:171], v[4:7]
	ds_read_b128 v[168:171], v16 offset:17600
	s_waitcnt lgkmcnt(7)
	v_mfma_f32_16x16x32_f16 v[0:3], v[80:83], v[8:11], v[0:3]
	s_waitcnt lgkmcnt(6)
	v_mfma_f32_16x16x32_f16 v[4:7], v[80:83], v[12:15], v[4:7]
	s_waitcnt lgkmcnt(5)
	v_mfma_f32_16x16x32_f16 v[0:3], v[84:87], v[20:23], v[0:3]
	s_waitcnt lgkmcnt(4)
	v_mfma_f32_16x16x32_f16 v[4:7], v[84:87], v[24:27], v[4:7]
	s_waitcnt lgkmcnt(3)
	v_mfma_f32_16x16x32_f16 v[0:3], v[88:91], v[28:31], v[0:3]
	s_waitcnt lgkmcnt(2)
	v_mfma_f32_16x16x32_f16 v[4:7], v[88:91], v[160:163], v[4:7]
	s_waitcnt lgkmcnt(1)
	v_mfma_f32_16x16x32_f16 v[0:3], v[92:95], v[164:167], v[0:3]
	s_waitcnt lgkmcnt(0)
	v_mfma_f32_16x16x32_f16 v[4:7], v[92:95], v[168:171], v[4:7]
	v_lshrrev_b32_e32 v17, 4, v189
	v_lshlrev_b32_e32 v17, 3, v17
	s_lshl_b32 s0, s3, 1
	v_add_u32_e32 v18, s74, v195
	v_lshl_add_u32 v17, v18, 7, v17
	v_add_u32_e32 v17, s0, v17
	v_readlane_b32 s4, v226, 0
	v_readlane_b32 s5, v226, 1
	s_mov_b32 s1, 0xc350
	v_add_u32_e32 v19, 16, v18
	v_lshlrev_b32_e32 v28, 2, v195
	s_nop 1
	v_cvt_pk_f16_f32 v20, v0, v1
	v_cvt_pk_f16_f32 v21, v2, v3
	v_cvt_pk_f16_f32 v22, v4, v5
	v_cvt_pk_f16_f32 v23, v6, v7
	v_cmp_gt_i32_e32 vcc, s1, v18
	v_cmp_gt_i32_e64 s[8:9], s1, v19
	v_mul_f32_e32 v24, v228, v0
	v_mul_f32_e32 v25, v232, v0
	v_mul_f32_e32 v26, v228, v4
	v_mul_f32_e32 v27, v232, v4
	v_fmac_f32_e32 v24, v229, v1
	v_fmac_f32_e32 v25, v233, v1
	v_fmac_f32_e32 v26, v229, v5
	v_fmac_f32_e32 v27, v233, v5
	v_fmac_f32_e32 v24, v230, v2
	v_fmac_f32_e32 v25, v234, v2
	v_fmac_f32_e32 v26, v230, v6
	v_fmac_f32_e32 v27, v234, v6
	v_fmac_f32_e32 v24, v231, v3
	v_fmac_f32_e32 v25, v235, v3
	v_fmac_f32_e32 v26, v231, v7
	v_fmac_f32_e32 v27, v235, v7
	s_mov_b64 exec, vcc
	global_store_dwordx2 v17, v[20:21], s[4:5]
	s_mov_b64 exec, s[8:9]
	global_store_dwordx2 v17, v[22:23], s[4:5] offset:2048
	s_mov_b64 exec, -1
	v_mov_b32_e32 v12, v24
	v_mov_b32_e32 v13, v25
	v_mov_b32_e32 v14, v26
	v_mov_b32_e32 v15, v27
	s_nop 1
	v_permlane32_swap_b32_e32 v24, v12
	v_permlane32_swap_b32_e32 v25, v13
	v_permlane32_swap_b32_e32 v26, v14
	v_permlane32_swap_b32_e32 v27, v15
	v_add_f32_e32 v24, v24, v12
	v_add_f32_e32 v25, v25, v13
	v_add_f32_e32 v26, v26, v14
	v_add_f32_e32 v27, v27, v15
	ds_swizzle_b32 v12, v24 offset:0x401f
	ds_swizzle_b32 v13, v25 offset:0x401f
	ds_swizzle_b32 v14, v26 offset:0x401f
	ds_swizzle_b32 v15, v27 offset:0x401f
	s_waitcnt lgkmcnt(0)
	v_add_f32_e32 v24, v24, v12
	v_add_f32_e32 v25, v25, v13
	v_add_f32_e32 v26, v26, v14
	v_add_f32_e32 v27, v27, v15
	s_lshl_b32 s0, s3, 4
	s_add_i32 s0, s0, 0xd3c0
	v_lshl_add_u32 v28, v195, 2, s0
	s_mov_b64 exec, 0xffff
	ds_write_b32 v28, v24
	ds_write_b32 v28, v26 offset:64
	ds_write_b32 v28, v25 offset:128
	ds_write_b32 v28, v27 offset:192
	s_mov_b64 exec, -1
	v_add_u32_e32 v1, s65, v189
	v_cmp_gt_i32_e32 vcc, 32, v1
	s_waitcnt lgkmcnt(0)
	s_barrier
	s_and_saveexec_b64 s[0:1], vcc
	s_cbranch_execz .LBB3_5
	v_add_u32_e32 v0, s74, v1
	s_mov_b32 s4, 0xc350
	v_lshlrev_b32_e32 v1, 2, v1
	v_cmp_gt_i32_e32 vcc, s4, v0
	v_add_u32_e32 v2, 0xd000, v1
	s_and_saveexec_b64 s[4:5], vcc
	s_cbranch_execz .LBB3_4
	v_add_u32_e32 v8, 0xd3c0, v1
	v_add_u32_e32 v9, 0xd440, v1
	ds_read2st64_b32 v[4:5], v8 offset1:1
	ds_read2st64_b32 v[10:11], v8 offset0:2 offset1:3
	ds_read2st64_b32 v[12:13], v9 offset1:1
	ds_read2st64_b32 v[14:15], v9 offset0:2 offset1:3
	v_ashrrev_i32_e32 v1, 31, v0
	v_readlane_b32 s8, v226, 0
	v_lshlrev_b64 v[0:1], 2, v[0:1]
	v_readlane_b32 s10, v226, 2
	v_readlane_b32 s11, v226, 3
	v_lshl_add_u64 v[6:7], s[76:77], 0, v[0:1]
	v_readlane_b32 s9, v226, 1
	v_lshl_add_u64 v[0:1], s[10:11], 0, v[0:1]
	s_waitcnt lgkmcnt(0)
	v_add_f32_e32 v5, v4, v5
	v_add_f32_e32 v10, v10, v11
	v_add_f32_e32 v4, v12, v13
	v_add_f32_e32 v12, v14, v15
	v_add_f32_e32 v5, v5, v10
	v_add_f32_e32 v4, v4, v12
	global_store_dword v[0:1], v5, off
	global_store_dword v[6:7], v4, off
	s_branch .LBB3_4

	.amdhsa_kernel _Z8k_layer1PKiS0_PKfS2_PK15HIP_vector_typeIjLj4EEPKDv8_DF16_S9_S2_S2_S2_PDF16_PfSB_
		.amdhsa_group_segment_fixed_size 55232
		.amdhsa_private_segment_fixed_size 0
		.amdhsa_kernarg_size 360
		.amdhsa_user_sgpr_count 2
		.amdhsa_user_sgpr_dispatch_ptr 0
		.amdhsa_user_sgpr_queue_ptr 0
		.amdhsa_user_sgpr_kernarg_segment_ptr 1
		.amdhsa_user_sgpr_dispatch_id 0
		.amdhsa_user_sgpr_kernarg_preload_length 0
		.amdhsa_user_sgpr_kernarg_preload_offset 0
		.amdhsa_user_sgpr_private_segment_size 0
		.amdhsa_uses_dynamic_stack 0
		.amdhsa_enable_private_segment 0
		.amdhsa_system_sgpr_workgroup_id_x 1
		.amdhsa_system_sgpr_workgroup_id_y 0
		.amdhsa_system_sgpr_workgroup_id_z 0
		.amdhsa_system_sgpr_workgroup_info 0
		.amdhsa_system_vgpr_workitem_id 0
		.amdhsa_next_free_vgpr 237
		.amdhsa_next_free_sgpr 100
		.amdhsa_accum_offset 240
		.amdhsa_reserve_vcc 1
		.amdhsa_float_round_mode_32 0
		.amdhsa_float_round_mode_16_64 0
		.amdhsa_float_denorm_mode_32 3
		.amdhsa_float_denorm_mode_16_64 3
		.amdhsa_dx10_clamp 1
		.amdhsa_ieee_mode 1
		.amdhsa_fp16_overflow 0
		.amdhsa_tg_split 0
		.amdhsa_exception_fp_ieee_invalid_op 0
		.amdhsa_exception_fp_denorm_src 0
		.amdhsa_exception_fp_ieee_div_zero 0
		.amdhsa_exception_fp_ieee_overflow 0
		.amdhsa_exception_fp_ieee_underflow 0
		.amdhsa_exception_fp_ieee_inexact 0
		.amdhsa_exception_int_div_zero 0
	.end_amdhsa_kernel

amdhsa.kernels:
  - .agpr_count:     0
    .args:
      - .actual_access:  read_only
        .address_space:  global
        .offset:         0
        .size:           8
        .value_kind:     global_buffer
      - .actual_access:  read_only
        .address_space:  global
        .offset:         8
        .size:           8
        .value_kind:     global_buffer
      - .actual_access:  read_only
        .address_space:  global
        .offset:         16
        .size:           8
        .value_kind:     global_buffer
      - .actual_access:  read_only
        .address_space:  global
        .offset:         24
        .size:           8
        .value_kind:     global_buffer
      - .actual_access:  read_only
        .address_space:  global
        .offset:         32
        .size:           8
        .value_kind:     global_buffer
      - .actual_access:  write_only
        .address_space:  global
        .offset:         40
        .size:           8
        .value_kind:     global_buffer
      - .actual_access:  write_only
        .address_space:  global
        .offset:         48
        .size:           8
        .value_kind:     global_buffer
      - .actual_access:  write_only
        .address_space:  global
        .offset:         56
        .size:           8
        .value_kind:     global_buffer
      - .actual_access:  write_only
        .address_space:  global
        .offset:         64
        .size:           8
        .value_kind:     global_buffer
    .group_segment_fixed_size: 1024
    .kernarg_segment_align: 8
    .kernarg_segment_size: 72
    .language:       OpenCL C
    .language_version:
      - 2
      - 0
    .max_flat_workgroup_size: 512
    .name:           _Z11k_hist_prepPKiPKfS2_S2_S2_PiPfPDF16_S5_
    .private_segment_fixed_size: 0
    .sgpr_count:     20
    .sgpr_spill_count: 0
    .symbol:         _Z11k_hist_prepPKiPKfS2_S2_S2_PiPfPDF16_S5_.kd
    .uniform_work_group_size: 1
    .uses_dynamic_stack: false
    .vgpr_count:     42
    .vgpr_spill_count: 0
    .wavefront_size: 64
  - .agpr_count:     0
    .args:
      - .actual_access:  read_only
        .address_space:  global
        .offset:         0
        .size:           8
        .value_kind:     global_buffer
      - .actual_access:  read_only
        .address_space:  global
        .offset:         8
        .size:           8
        .value_kind:     global_buffer
      - .actual_access:  write_only
        .address_space:  global
        .offset:         16
        .size:           8
        .value_kind:     global_buffer
      - .actual_access:  write_only
        .address_space:  global
        .offset:         24
        .size:           8
        .value_kind:     global_buffer
      - .actual_access:  read_only
        .address_space:  global
        .offset:         32
        .size:           8
        .value_kind:     global_buffer
      - .actual_access:  read_only
        .address_space:  global
        .offset:         40
        .size:           8
        .value_kind:     global_buffer
      - .actual_access:  write_only
        .address_space:  global
        .offset:         48
        .size:           8
        .value_kind:     global_buffer
      - .actual_access:  write_only
        .address_space:  global
        .offset:         56
        .size:           8
        .value_kind:     global_buffer
      - .actual_access:  write_only
        .address_space:  global
        .offset:         64
        .size:           8
        .value_kind:     global_buffer
    .group_segment_fixed_size: 9344
    .kernarg_segment_align: 8
    .kernarg_segment_size: 72
    .language:       OpenCL C
    .language_version:
      - 2
      - 0
    .max_flat_workgroup_size: 512
    .name:           _Z14k_scatter_nodePKiS0_PjPiPKfS4_PfS5_PDF16_
    .private_segment_fixed_size: 0
    .sgpr_count:     106
    .sgpr_spill_count: 10
    .symbol:         _Z14k_scatter_nodePKiS0_PjPiPKfS4_PfS5_PDF16_.kd
    .uniform_work_group_size: 1
    .uses_dynamic_stack: false
    .vgpr_count:     118
    .vgpr_spill_count: 0
    .wavefront_size: 64
  - .agpr_count:     0
    .args:
      - .actual_access:  read_only
        .address_space:  global
        .offset:         0
        .size:           8
        .value_kind:     global_buffer
      - .actual_access:  read_only
        .address_space:  global
        .offset:         8
        .size:           8
        .value_kind:     global_buffer
      - .actual_access:  write_only
        .address_space:  global
        .offset:         16
        .size:           8
        .value_kind:     global_buffer
      - .actual_access:  write_only
        .address_space:  global
        .offset:         24
        .size:           8
        .value_kind:     global_buffer
    .group_segment_fixed_size: 3072
    .kernarg_segment_align: 8
    .kernarg_segment_size: 32
    .language:       OpenCL C
    .language_version:
      - 2
      - 0
    .max_flat_workgroup_size: 1024
    .name:           _Z5k_csrPKjPKiPiS3_
    .private_segment_fixed_size: 0
    .sgpr_count:     34
    .sgpr_spill_count: 0
    .symbol:         _Z5k_csrPKjPKiPiS3_.kd
    .uniform_work_group_size: 1
    .uses_dynamic_stack: false
    .vgpr_count:     18
    .vgpr_spill_count: 0
    .wavefront_size: 64
  - .agpr_count:     0
    .args:
      - .actual_access:  read_only
        .address_space:  global
        .offset:         0
        .size:           8
        .value_kind:     global_buffer
      - .actual_access:  read_only
        .address_space:  global
        .offset:         8
        .size:           8
        .value_kind:     global_buffer
      - .actual_access:  read_only
        .address_space:  global
        .offset:         16
        .size:           8
        .value_kind:     global_buffer
      - .actual_access:  read_only
        .address_space:  global
        .offset:         24
        .size:           8
        .value_kind:     global_buffer
      - .actual_access:  read_only
        .address_space:  global
        .offset:         32
        .size:           8
        .value_kind:     global_buffer
      - .actual_access:  read_only
        .address_space:  global
        .offset:         40
        .size:           8
        .value_kind:     global_buffer
      - .actual_access:  read_only
        .address_space:  global
        .offset:         48
        .size:           8
        .value_kind:     global_buffer
      - .actual_access:  read_only
        .address_space:  global
        .offset:         56
        .size:           8
        .value_kind:     global_buffer
      - .actual_access:  read_only
        .address_space:  global
        .offset:         64
        .size:           8
        .value_kind:     global_buffer
      - .actual_access:  read_only
        .address_space:  global
        .offset:         72
        .size:           8
        .value_kind:     global_buffer
      - .actual_access:  write_only
        .address_space:  global
        .offset:         80
        .size:           8
        .value_kind:     global_buffer
      - .actual_access:  write_only
        .address_space:  global
        .offset:         88
        .size:           8
        .value_kind:     global_buffer
      - .actual_access:  write_only
        .address_space:  global
        .offset:         96
        .size:           8
        .value_kind:     global_buffer
      - .offset:         104
        .size:           4
        .value_kind:     hidden_block_count_x
      - .offset:         108
        .size:           4
        .value_kind:     hidden_block_count_y
      - .offset:         112
        .size:           4
        .value_kind:     hidden_block_count_z
      - .offset:         116
        .size:           2
        .value_kind:     hidden_group_size_x
      - .offset:         118
        .size:           2
        .value_kind:     hidden_group_size_y
      - .offset:         120
        .size:           2
        .value_kind:     hidden_group_size_z
      - .offset:         122
        .size:           2
        .value_kind:     hidden_remainder_x
      - .offset:         124
        .size:           2
        .value_kind:     hidden_remainder_y
      - .offset:         126
        .size:           2
        .value_kind:     hidden_remainder_z
      - .offset:         144
        .size:           8
        .value_kind:     hidden_global_offset_x
      - .offset:         152
        .size:           8
        .value_kind:     hidden_global_offset_y
      - .offset:         160
        .size:           8
        .value_kind:     hidden_global_offset_z
      - .offset:         168
        .size:           2
        .value_kind:     hidden_grid_dims
    .group_segment_fixed_size: 55232
    .kernarg_segment_align: 8
    .kernarg_segment_size: 360
    .language:       OpenCL C
    .language_version:
      - 2
      - 0
    .max_flat_workgroup_size: 256
    .name:           _Z8k_layer1PKiS0_PKfS2_PK15HIP_vector_typeIjLj4EEPKDv8_DF16_S9_S2_S2_S2_PDF16_PfSB_
    .private_segment_fixed_size: 0
    .sgpr_count:     106
    .sgpr_spill_count: 7
    .symbol:         _Z8k_layer1PKiS0_PKfS2_PK15HIP_vector_typeIjLj4EEPKDv8_DF16_S9_S2_S2_S2_PDF16_PfSB_.kd
    .uniform_work_group_size: 1
    .uses_dynamic_stack: false
    .vgpr_count:     237
    .vgpr_spill_count: 0
    .wavefront_size: 64
  - .agpr_count:     0
    .args:
      - .actual_access:  read_only
        .address_space:  global
        .offset:         0
        .size:           8
        .value_kind:     global_buffer
      - .actual_access:  read_only
        .address_space:  global
        .offset:         8
        .size:           8
        .value_kind:     global_buffer
      - .actual_access:  read_only
        .address_space:  global
        .offset:         16
        .size:           8
        .value_kind:     global_buffer
      - .actual_access:  read_only
        .address_space:  global
        .offset:         24
        .size:           8
        .value_kind:     global_buffer
      - .actual_access:  read_only
        .address_space:  global
        .offset:         32
        .size:           8
        .value_kind:     global_buffer
      - .actual_access:  read_only
        .address_space:  global
        .offset:         40
        .size:           8
        .value_kind:     global_buffer
      - .actual_access:  write_only
        .address_space:  global
        .offset:         48
        .size:           8
        .value_kind:     global_buffer
    .group_segment_fixed_size: 0
    .kernarg_segment_align: 8
    .kernarg_segment_size: 56
    .language:       OpenCL C
    .language_version:
      - 2
      - 0
    .max_flat_workgroup_size: 256
    .name:           _Z8k_layer2PKiS0_PKfS2_PK15HIP_vector_typeIjLj4EES2_Pf
    .private_segment_fixed_size: 0
    .sgpr_count:     52
    .sgpr_spill_count: 0
    .symbol:         _Z8k_layer2PKiS0_PKfS2_PK15HIP_vector_typeIjLj4EES2_Pf.kd
    .uniform_work_group_size: 1
    .uses_dynamic_stack: false
    .vgpr_count:     70
    .vgpr_spill_count: 0
    .wavefront_size: 64
